# v76 + attention combo: alias waits before V reads removed, SWA sink load off the K/V DMA critical path, SWA O rescaled in place (no back-edge phi copies)
# speedup vs baseline: 1.0107x; 1.0091x over previous
.LBB0_3630:
	v_exp_f32_e32 v0, v34
	v_exp_f32_e32 v90, v50
	v_exp_f32_e32 v91, v35
	v_exp_f32_e32 v92, v51
	v_exp_f32_e32 v93, v36
	v_exp_f32_e32 v94, v52
	v_exp_f32_e32 v95, v37
	v_exp_f32_e32 v96, v53
	v_add_f32_e32 v34, 0, v0
	v_add_f32_e32 v50, 0, v90
	v_add_f32_e32 v34, v91, v34
	v_add_f32_e32 v35, v92, v50
	v_add_f32_e32 v34, v93, v34
	v_add_f32_e32 v36, v94, v35
	v_add_f32_e32 v35, v95, v34
	v_add_f32_e32 v34, v96, v36
	v_exp_f32_e32 v37, v38
	v_exp_f32_e32 v36, v54
	v_exp_f32_e32 v39, v39
	v_exp_f32_e32 v38, v55
	v_exp_f32_e32 v51, v40
	v_exp_f32_e32 v50, v56
	v_exp_f32_e32 v41, v41
	v_exp_f32_e32 v40, v57
	v_exp_f32_e32 v53, v42
	v_exp_f32_e32 v52, v58
	v_pk_add_f32 v[34:35], v[36:37], v[34:35]
	v_exp_f32_e32 v55, v43
	v_exp_f32_e32 v54, v59
	v_pk_add_f32 v[34:35], v[38:39], v[34:35]
	v_exp_f32_e32 v57, v44
	v_exp_f32_e32 v56, v60
	v_pk_add_f32 v[34:35], v[50:51], v[34:35]
	v_exp_f32_e32 v59, v45
	v_exp_f32_e32 v58, v61
	v_pk_add_f32 v[34:35], v[40:41], v[34:35]
	v_exp_f32_e32 v61, v46
	v_exp_f32_e32 v60, v62
	v_pk_add_f32 v[34:35], v[52:53], v[34:35]
	v_exp_f32_e32 v87, v47
	v_exp_f32_e32 v86, v63
	v_pk_add_f32 v[34:35], v[54:55], v[34:35]
	v_exp_f32_e32 v63, v48
	v_exp_f32_e32 v62, v64
	v_exp_f32_e32 v89, v49
	v_exp_f32_e32 v88, v65
	v_pk_add_f32 v[34:35], v[56:57], v[34:35]
	v_cvt_pk_bf16_f32 v46, v0, v91
	v_pk_add_f32 v[34:35], v[58:59], v[34:35]
	v_add_u32_e32 v0, s0, v125
	v_pk_add_f32 v[34:35], v[60:61], v[34:35]
	v_add3_u32 v0, v0, v126, v122
	v_pk_add_f32 v[34:35], v[86:87], v[34:35]
	v_cvt_pk_bf16_f32 v49, v51, v41
	v_pk_add_f32 v[34:35], v[62:63], v[34:35]
	v_cvt_pk_bf16_f32 v45, v63, v89
	v_cvt_pk_bf16_f32 v41, v62, v88
	ds_read_b64_tr_b16 v[62:63], v0 offset:16384
	ds_read_b64_tr_b16 v[64:65], v0 offset:16896
	v_pk_add_f32 v[34:35], v[88:89], v[34:35]
	v_cvt_pk_bf16_f32 v47, v93, v95
	v_add_f32_e32 v34, v34, v35
	v_cvt_pk_bf16_f32 v48, v37, v39
	v_cvt_pk_bf16_f32 v44, v61, v87
	v_cvt_pk_bf16_f32 v37, v50, v40
	v_cvt_pk_bf16_f32 v40, v60, v86
	ds_read_b64_tr_b16 v[86:87], v0 offset:17408
	ds_read_b64_tr_b16 v[88:89], v0 offset:17920
	v_add_f32_e32 v120, v120, v34
	v_cvt_pk_bf16_f32 v34, v90, v92
	ds_read_b64_tr_b16 v[90:91], v0 offset:18432
	ds_read_b64_tr_b16 v[92:93], v0 offset:18944
	s_waitcnt lgkmcnt(4)
	v_mfma_f32_32x32x16_bf16 v[2:17], v[62:65], v[46:49], v[2:17]
	v_cvt_pk_bf16_f32 v42, v53, v55
	v_cvt_pk_bf16_f32 v43, v57, v59
	v_cvt_pk_bf16_f32 v35, v94, v96
	ds_read_b64_tr_b16 v[94:95], v0 offset:19456
	ds_read_b64_tr_b16 v[96:97], v0 offset:19968
	v_cvt_pk_bf16_f32 v36, v36, v38
	v_cvt_pk_bf16_f32 v38, v52, v54
	s_waitcnt lgkmcnt(4)
	v_mfma_f32_32x32x16_bf16 v[2:17], v[86:89], v[42:45], v[2:17]
	ds_read_b64_tr_b16 v[98:99], v0 offset:20480
	ds_read_b64_tr_b16 v[100:101], v0 offset:20992
	v_cvt_pk_bf16_f32 v39, v56, v58
	s_xor_b32 s2, s2, 1
	s_cmp_lt_i32 s47, 0
	s_waitcnt lgkmcnt(4)
	v_mfma_f32_32x32x16_bf16 v[2:17], v[90:93], v[34:37], v[2:17]
	ds_read_b64_tr_b16 v[58:59], v0 offset:21504
	ds_read_b64_tr_b16 v[60:61], v0 offset:22016
	s_waitcnt lgkmcnt(4)
	v_mfma_f32_32x32x16_bf16 v[2:17], v[94:97], v[38:41], v[2:17]
	ds_read_b64_tr_b16 v[50:51], v0 offset:22528
	ds_read_b64_tr_b16 v[52:53], v0 offset:23040
	s_waitcnt lgkmcnt(4)
	v_mfma_f32_32x32x16_bf16 v[18:33], v[98:101], v[46:49], v[18:33]
	ds_read_b64_tr_b16 v[54:55], v0 offset:23552
	ds_read_b64_tr_b16 v[56:57], v0 offset:24064
	s_waitcnt lgkmcnt(4)
	v_mfma_f32_32x32x16_bf16 v[18:33], v[58:61], v[42:45], v[18:33]
	s_waitcnt lgkmcnt(2)
	v_mfma_f32_32x32x16_bf16 v[18:33], v[50:53], v[34:37], v[18:33]
	s_waitcnt lgkmcnt(0)
	v_mfma_f32_32x32x16_bf16 v[18:33], v[54:57], v[38:41], v[18:33]
	s_cbranch_scc1 .LBB0_3633
	s_mov_b32 s8, s47
	s_branch .LBB0_3619
